# baseline (speedup 1.0000x reference)
_Z8gemm_f16ILi256ELi160ELi4ELi2ELi2ELi1ELi1EEvPKDF16_S1_Pviiii:
	s_load_dwordx4 s[12:15], s[0:1], 0x0
	s_load_dwordx2 s[0:1], s[0:1], 0x10
	s_and_b32 s3, s2, 3
	s_mul_i32 s3, s3, 30
	s_lshr_b32 s6, s2, 3
	s_add_i32 s3, s3, s6
	s_and_b32 s6, s2, 4
	s_and_b32 s7, s3, 3
	s_or_b32 s6, s6, s7
	s_lshl_b32 s10, s6, 8
	s_lshr_b32 s2, s3, 2
	s_cmp_eq_u32 s2, 29
	s_cbranch_scc1 .Lg1_pad_exit
	s_mulk_i32 s2, 0xa0
	s_movk_i32 s5, 0x12c0
	v_lshrrev_b32_e32 v95, 3, v0
	v_and_b32_e32 v99, 7, v0
	v_bfe_u32 v91, v0, 4, 3
	v_xor_b32_e32 v99, v99, v91
	v_lshlrev_b32_e32 v99, 4, v99
	v_add_u32_e32 v91, s10, v95
	v_lshl_add_u32 v82, v91, 11, v99
	v_add_u32_e32 v83, 0x20000, v82
	v_add_u32_e32 v84, 0x40000, v82
	v_add_u32_e32 v85, 0x60000, v82
	v_add_u32_e32 v91, s2, v95
	v_lshl_add_u32 v86, v91, 11, v99
	v_add_u32_e32 v87, 0x20000, v86
	v_add_u32_e32 v88, 0x40000, v86
	v_lshlrev_b32_e32 v95, 4, v0
	s_nop 0
	v_readfirstlane_b32 s20, v95
	s_mov_b32 s29, 0xa000
	s_cmp_lt_u32 s20, 0x1000
	s_cselect_b32 s29, 0xc000, s29
	s_cbranch_scc1 .Lg1_w03
	v_mov_b32_e32 v88, v87
.Lg1_w03:
	v_and_b32_e32 v98, 15, v0
	v_bfe_u32 v97, v0, 4, 2
	v_lshrrev_b32_e32 v96, 7, v0
	v_bfe_u32 v1, v0, 6, 1
	v_bfe_u32 v95, v0, 1, 3
	v_xor_b32_e32 v95, v97, v95
	v_lshlrev_b32_e32 v95, 4, v95
	v_lshl_or_b32 v99, v98, 7, v95
	v_lshl_or_b32 v89, v96, 13, v99
	v_mul_u32_u24_e32 v95, 0x2800, v1
	v_add_u32_e32 v95, 0x8000, v95
	v_add_u32_e32 v90, v95, v99
	s_waitcnt lgkmcnt(0)
	s_mov_b32 s22, s12
	s_mov_b32 s23, s13
	s_mov_b32 s24, s14
	s_mov_b32 s25, s15
	s_mov_b32 s26, s20
	s_add_i32 s30, s26, s29
	s_mov_b32 m0, s26
	s_add_i32 s26, s26, 0x2000
	global_load_lds_dwordx4 v82, s[22:23]
	s_mov_b32 m0, s26
	s_add_i32 s26, s26, 0x2000
	global_load_lds_dwordx4 v83, s[22:23]
	s_mov_b32 m0, s26
	s_add_i32 s26, s26, 0x2000
	global_load_lds_dwordx4 v84, s[22:23]
	s_mov_b32 m0, s26
	s_add_i32 s26, s26, 0x2000
	global_load_lds_dwordx4 v85, s[22:23]
	s_mov_b32 m0, s26
	s_add_i32 s26, s26, 0x2000
	global_load_lds_dwordx4 v86, s[24:25]
	s_mov_b32 m0, s26
	s_add_i32 s26, s26, 0x2000
	global_load_lds_dwordx4 v87, s[24:25]
	s_mov_b32 m0, s30
	s_add_i32 s26, s26, 0x1000
	global_load_lds_dwordx4 v88, s[24:25]
	s_add_u32 s22, s22, 0x80
	s_addc_u32 s23, s23, 0
	s_add_u32 s24, s24, 0x80
	s_addc_u32 s25, s25, 0
	s_add_i32 s30, s26, s29
	s_mov_b32 m0, s26
	s_add_i32 s26, s26, 0x2000
	global_load_lds_dwordx4 v82, s[22:23]
	s_mov_b32 m0, s26
	s_add_i32 s26, s26, 0x2000
	global_load_lds_dwordx4 v83, s[22:23]
	s_mov_b32 m0, s26
	s_add_i32 s26, s26, 0x2000
	global_load_lds_dwordx4 v84, s[22:23]
	s_mov_b32 m0, s26
	s_add_i32 s26, s26, 0x2000
	global_load_lds_dwordx4 v85, s[22:23]
	s_mov_b32 m0, s26
	s_add_i32 s26, s26, 0x2000
	global_load_lds_dwordx4 v86, s[24:25]
	s_mov_b32 m0, s26
	s_add_i32 s26, s26, 0x2000
	global_load_lds_dwordx4 v87, s[24:25]
	s_mov_b32 m0, s30
	s_add_i32 s26, s26, 0x1000
	global_load_lds_dwordx4 v88, s[24:25]
	s_add_u32 s22, s22, 0x80
	s_addc_u32 s23, s23, 0
	s_add_u32 s24, s24, 0x80
	s_addc_u32 s25, s25, 0
	s_add_i32 s30, s26, s29
	s_mov_b32 m0, s26
	s_add_i32 s26, s26, 0x2000
	global_load_lds_dwordx4 v82, s[22:23]
	s_mov_b32 m0, s26
	s_add_i32 s26, s26, 0x2000
	global_load_lds_dwordx4 v83, s[22:23]
	s_mov_b32 m0, s26
	s_add_i32 s26, s26, 0x2000
	global_load_lds_dwordx4 v84, s[22:23]
	s_mov_b32 m0, s26
	s_add_i32 s26, s26, 0x2000
	global_load_lds_dwordx4 v85, s[22:23]
	s_mov_b32 m0, s26
	s_add_i32 s26, s26, 0x2000
	global_load_lds_dwordx4 v86, s[24:25]
	s_mov_b32 m0, s26
	s_add_i32 s26, s26, 0x2000
	global_load_lds_dwordx4 v87, s[24:25]
	s_mov_b32 m0, s30
	s_add_i32 s26, s26, 0x1000
	global_load_lds_dwordx4 v88, s[24:25]
	v_mov_b32_e32 v2, 0
	v_mov_b32_e32 v3, 0
	v_mov_b32_e32 v4, 0
	v_mov_b32_e32 v5, 0
	v_mov_b32_e32 v6, 0
	v_mov_b32_e32 v7, 0
	v_mov_b32_e32 v8, 0
	v_mov_b32_e32 v9, 0
	v_mov_b32_e32 v10, 0
	v_mov_b32_e32 v11, 0
	v_mov_b32_e32 v12, 0
	v_mov_b32_e32 v13, 0
	v_mov_b32_e32 v14, 0
	v_mov_b32_e32 v15, 0
	v_mov_b32_e32 v16, 0
	v_mov_b32_e32 v17, 0
	v_mov_b32_e32 v18, 0
	v_mov_b32_e32 v19, 0
	v_mov_b32_e32 v20, 0
	v_mov_b32_e32 v21, 0
	v_mov_b32_e32 v22, 0
	v_mov_b32_e32 v23, 0
	v_mov_b32_e32 v24, 0
	v_mov_b32_e32 v25, 0
	v_mov_b32_e32 v26, 0
	v_mov_b32_e32 v27, 0
	v_mov_b32_e32 v28, 0
	v_mov_b32_e32 v29, 0
	v_mov_b32_e32 v30, 0
	v_mov_b32_e32 v31, 0
	v_mov_b32_e32 v32, 0
	v_mov_b32_e32 v33, 0
	v_mov_b32_e32 v34, 0
	v_mov_b32_e32 v35, 0
	v_mov_b32_e32 v36, 0
	v_mov_b32_e32 v37, 0
	v_mov_b32_e32 v38, 0
	v_mov_b32_e32 v39, 0
	v_mov_b32_e32 v40, 0
	v_mov_b32_e32 v41, 0
	v_mov_b32_e32 v42, 0
	v_mov_b32_e32 v43, 0
	v_mov_b32_e32 v44, 0
	v_mov_b32_e32 v45, 0
	v_mov_b32_e32 v46, 0
	v_mov_b32_e32 v47, 0
	v_mov_b32_e32 v48, 0
	v_mov_b32_e32 v49, 0
	v_mov_b32_e32 v50, 0
	v_mov_b32_e32 v51, 0
	v_mov_b32_e32 v52, 0
	v_mov_b32_e32 v53, 0
	v_mov_b32_e32 v54, 0
	v_mov_b32_e32 v55, 0
	v_mov_b32_e32 v56, 0
	v_mov_b32_e32 v57, 0
	v_mov_b32_e32 v58, 0
	v_mov_b32_e32 v59, 0
	v_mov_b32_e32 v60, 0
	v_mov_b32_e32 v61, 0
	v_mov_b32_e32 v62, 0
	v_mov_b32_e32 v63, 0
	v_mov_b32_e32 v64, 0
	v_mov_b32_e32 v65, 0
	v_mov_b32_e32 v66, 0
	v_mov_b32_e32 v67, 0
	v_mov_b32_e32 v68, 0
	v_mov_b32_e32 v69, 0
	v_mov_b32_e32 v70, 0
	v_mov_b32_e32 v71, 0
	v_mov_b32_e32 v72, 0
	v_mov_b32_e32 v73, 0
	v_mov_b32_e32 v74, 0
	v_mov_b32_e32 v75, 0
	v_mov_b32_e32 v76, 0
	v_mov_b32_e32 v77, 0
	v_mov_b32_e32 v78, 0
	v_mov_b32_e32 v79, 0
	v_mov_b32_e32 v80, 0
	v_mov_b32_e32 v81, 0
	s_mov_b32 s16, 0
	s_mov_b32 s17, 0
	v_mov_b32_e32 v91, v89
	v_mov_b32_e32 v93, v90
	v_xor_b32_e32 v92, 64, v89
	v_xor_b32_e32 v94, 64, v90
	s_waitcnt vmcnt(14)
	s_barrier
	ds_read_b128 v[116:119], v93
	ds_read_b128 v[100:103], v91
	ds_read_b128 v[120:123], v93 offset:2048
	ds_read_b128 v[104:107], v91 offset:2048
	ds_read_b128 v[124:127], v93 offset:4096
	ds_read_b128 v[108:111], v91 offset:4096
	ds_read_b128 v[128:131], v93 offset:6144
	ds_read_b128 v[112:115], v91 offset:6144
	ds_read_b128 v[132:135], v93 offset:8192
	s_add_i32 s27, s17, 0xd000
	s_cmp_lg_u32 s27, 0x27000
	s_cselect_b32 s27, s27, 0
	s_waitcnt lgkmcnt(0)
	v_mfma_f32_16x16x32_f16 v[34:37], v[116:119], v[100:103], v[34:37]
	ds_read_b128 v[152:155], v94
	v_mfma_f32_16x16x32_f16 v[78:81], v[120:123], v[100:103], v[78:81]
	ds_read_b128 v[136:139], v92
	v_mfma_f32_16x16x32_f16 v[74:77], v[124:127], v[100:103], v[74:77]
	ds_read_b128 v[156:159], v94 offset:2048
	v_mfma_f32_16x16x32_f16 v[70:73], v[128:131], v[100:103], v[70:73]
	ds_read_b128 v[140:143], v92 offset:2048
	v_mfma_f32_16x16x32_f16 v[62:65], v[132:135], v[100:103], v[62:65]
	ds_read_b128 v[160:163], v94 offset:4096
	v_mfma_f32_16x16x32_f16 v[58:61], v[116:119], v[104:107], v[58:61]
	ds_read_b128 v[144:147], v92 offset:4096
	v_mfma_f32_16x16x32_f16 v[54:57], v[120:123], v[104:107], v[54:57]
	ds_read_b128 v[164:167], v94 offset:6144
	v_mfma_f32_16x16x32_f16 v[50:53], v[124:127], v[104:107], v[50:53]
	ds_read_b128 v[148:151], v92 offset:6144
	v_mfma_f32_16x16x32_f16 v[46:49], v[128:131], v[104:107], v[46:49]
	ds_read_b128 v[168:171], v94 offset:8192
	v_mfma_f32_16x16x32_f16 v[42:45], v[132:135], v[104:107], v[42:45]
	v_mfma_f32_16x16x32_f16 v[38:41], v[116:119], v[108:111], v[38:41]
	v_add_u32_e32 v91, s27, v89
	v_mfma_f32_16x16x32_f16 v[30:33], v[120:123], v[108:111], v[30:33]
	v_add_u32_e32 v93, s27, v90
	v_mfma_f32_16x16x32_f16 v[26:29], v[124:127], v[108:111], v[26:29]
	v_xor_b32_e32 v92, 64, v91
	v_mfma_f32_16x16x32_f16 v[22:25], v[128:131], v[108:111], v[22:25]
	v_xor_b32_e32 v94, 64, v93
	v_mfma_f32_16x16x32_f16 v[18:21], v[132:135], v[108:111], v[18:21]
	v_mfma_f32_16x16x32_f16 v[14:17], v[116:119], v[112:115], v[14:17]
	v_mfma_f32_16x16x32_f16 v[10:13], v[120:123], v[112:115], v[10:13]
	v_mfma_f32_16x16x32_f16 v[2:5], v[124:127], v[112:115], v[2:5]
	v_mfma_f32_16x16x32_f16 v[6:9], v[128:131], v[112:115], v[6:9]
	v_mfma_f32_16x16x32_f16 v[66:69], v[132:135], v[112:115], v[66:69]
	s_add_i32 s18, s16, 3
	s_lshl_b32 s18, s18, 7
	s_add_u32 s22, s12, s18
	s_addc_u32 s23, s13, 0
	s_add_u32 s24, s14, s18
	s_addc_u32 s25, s15, 0
	s_add_i32 s26, s17, s20
	s_add_i32 s30, s26, s29
	s_waitcnt vmcnt(7)
	s_waitcnt lgkmcnt(0)
	s_barrier
	s_mov_b32 m0, s26
	v_mfma_f32_16x16x32_f16 v[34:37], v[152:155], v[136:139], v[34:37]
	ds_read_b128 v[116:119], v93
	v_mfma_f32_16x16x32_f16 v[78:81], v[156:159], v[136:139], v[78:81]
	ds_read_b128 v[100:103], v91
	v_mfma_f32_16x16x32_f16 v[74:77], v[160:163], v[136:139], v[74:77]
	ds_read_b128 v[120:123], v93 offset:2048
	v_mfma_f32_16x16x32_f16 v[70:73], v[164:167], v[136:139], v[70:73]
	ds_read_b128 v[104:107], v91 offset:2048
	v_mfma_f32_16x16x32_f16 v[62:65], v[168:171], v[136:139], v[62:65]
	ds_read_b128 v[124:127], v93 offset:4096
	v_mfma_f32_16x16x32_f16 v[58:61], v[152:155], v[140:143], v[58:61]
	ds_read_b128 v[108:111], v91 offset:4096
	v_mfma_f32_16x16x32_f16 v[54:57], v[156:159], v[140:143], v[54:57]
	ds_read_b128 v[128:131], v93 offset:6144
	v_mfma_f32_16x16x32_f16 v[50:53], v[160:163], v[140:143], v[50:53]
	ds_read_b128 v[112:115], v91 offset:6144
	v_mfma_f32_16x16x32_f16 v[46:49], v[164:167], v[140:143], v[46:49]
	ds_read_b128 v[132:135], v93 offset:8192
	v_mfma_f32_16x16x32_f16 v[42:45], v[168:171], v[140:143], v[42:45]
	v_mfma_f32_16x16x32_f16 v[38:41], v[152:155], v[144:147], v[38:41]
	global_load_lds_dwordx4 v82, s[22:23]
	s_add_u32 m0, m0, 0x2000
	v_mfma_f32_16x16x32_f16 v[30:33], v[156:159], v[144:147], v[30:33]
	v_mfma_f32_16x16x32_f16 v[26:29], v[160:163], v[144:147], v[26:29]
	v_mfma_f32_16x16x32_f16 v[22:25], v[164:167], v[144:147], v[22:25]
	global_load_lds_dwordx4 v83, s[22:23]
	s_add_u32 m0, m0, 0x2000
	v_mfma_f32_16x16x32_f16 v[18:21], v[168:171], v[144:147], v[18:21]
	v_mfma_f32_16x16x32_f16 v[14:17], v[152:155], v[148:151], v[14:17]
	v_mfma_f32_16x16x32_f16 v[10:13], v[156:159], v[148:151], v[10:13]
	global_load_lds_dwordx4 v84, s[22:23]
	s_add_u32 m0, m0, 0x2000
	v_mfma_f32_16x16x32_f16 v[2:5], v[160:163], v[148:151], v[2:5]
	v_mfma_f32_16x16x32_f16 v[6:9], v[164:167], v[148:151], v[6:9]
	v_mfma_f32_16x16x32_f16 v[66:69], v[168:171], v[148:151], v[66:69]
	global_load_lds_dwordx4 v85, s[22:23]
	s_add_u32 m0, m0, 0x2000
	s_mov_b32 s17, s27
	s_add_i32 s16, s16, 1
.Lg1_loop:
	s_add_i32 s27, s17, 0xd000
	s_cmp_lg_u32 s27, 0x27000
	s_cselect_b32 s27, s27, 0
	s_waitcnt lgkmcnt(0)
	v_mfma_f32_16x16x32_f16 v[34:37], v[116:119], v[100:103], v[34:37]
	ds_read_b128 v[152:155], v94
	v_mfma_f32_16x16x32_f16 v[78:81], v[120:123], v[100:103], v[78:81]
	ds_read_b128 v[136:139], v92
	v_mfma_f32_16x16x32_f16 v[74:77], v[124:127], v[100:103], v[74:77]
	ds_read_b128 v[156:159], v94 offset:2048
	v_mfma_f32_16x16x32_f16 v[70:73], v[128:131], v[100:103], v[70:73]
	ds_read_b128 v[140:143], v92 offset:2048
	v_mfma_f32_16x16x32_f16 v[62:65], v[132:135], v[100:103], v[62:65]
	ds_read_b128 v[160:163], v94 offset:4096
	v_mfma_f32_16x16x32_f16 v[58:61], v[116:119], v[104:107], v[58:61]
	ds_read_b128 v[144:147], v92 offset:4096
	v_mfma_f32_16x16x32_f16 v[54:57], v[120:123], v[104:107], v[54:57]
	ds_read_b128 v[164:167], v94 offset:6144
	v_mfma_f32_16x16x32_f16 v[50:53], v[124:127], v[104:107], v[50:53]
	ds_read_b128 v[148:151], v92 offset:6144
	v_mfma_f32_16x16x32_f16 v[46:49], v[128:131], v[104:107], v[46:49]
	ds_read_b128 v[168:171], v94 offset:8192
	v_mfma_f32_16x16x32_f16 v[42:45], v[132:135], v[104:107], v[42:45]
	v_mfma_f32_16x16x32_f16 v[38:41], v[116:119], v[108:111], v[38:41]
	v_add_u32_e32 v91, s27, v89
	v_mfma_f32_16x16x32_f16 v[30:33], v[120:123], v[108:111], v[30:33]
	v_add_u32_e32 v93, s27, v90
	v_mfma_f32_16x16x32_f16 v[26:29], v[124:127], v[108:111], v[26:29]
	v_xor_b32_e32 v92, 64, v91
	v_mfma_f32_16x16x32_f16 v[22:25], v[128:131], v[108:111], v[22:25]
	v_xor_b32_e32 v94, 64, v93
	v_mfma_f32_16x16x32_f16 v[18:21], v[132:135], v[108:111], v[18:21]
	global_load_lds_dwordx4 v86, s[24:25]
	s_add_u32 m0, m0, 0x2000
	v_mfma_f32_16x16x32_f16 v[14:17], v[116:119], v[112:115], v[14:17]
	v_mfma_f32_16x16x32_f16 v[10:13], v[120:123], v[112:115], v[10:13]
	global_load_lds_dwordx4 v87, s[24:25]
	s_mov_b32 m0, s30
	v_mfma_f32_16x16x32_f16 v[2:5], v[124:127], v[112:115], v[2:5]
	v_mfma_f32_16x16x32_f16 v[6:9], v[128:131], v[112:115], v[6:9]
	global_load_lds_dwordx4 v88, s[24:25]
	v_mfma_f32_16x16x32_f16 v[66:69], v[132:135], v[112:115], v[66:69]
	s_add_i32 s18, s16, 3
	s_lshl_b32 s18, s18, 7
	s_add_u32 s22, s12, s18
	s_addc_u32 s23, s13, 0
	s_add_u32 s24, s14, s18
	s_addc_u32 s25, s15, 0
	s_add_i32 s26, s17, s20
	s_add_i32 s30, s26, s29
	s_waitcnt vmcnt(7)
	s_waitcnt lgkmcnt(0)
	s_barrier
	s_mov_b32 m0, s26
	v_mfma_f32_16x16x32_f16 v[34:37], v[152:155], v[136:139], v[34:37]
	ds_read_b128 v[116:119], v93
	v_mfma_f32_16x16x32_f16 v[78:81], v[156:159], v[136:139], v[78:81]
	ds_read_b128 v[100:103], v91
	v_mfma_f32_16x16x32_f16 v[74:77], v[160:163], v[136:139], v[74:77]
	ds_read_b128 v[120:123], v93 offset:2048
	v_mfma_f32_16x16x32_f16 v[70:73], v[164:167], v[136:139], v[70:73]
	ds_read_b128 v[104:107], v91 offset:2048
	v_mfma_f32_16x16x32_f16 v[62:65], v[168:171], v[136:139], v[62:65]
	ds_read_b128 v[124:127], v93 offset:4096
	v_mfma_f32_16x16x32_f16 v[58:61], v[152:155], v[140:143], v[58:61]
	ds_read_b128 v[108:111], v91 offset:4096
	v_mfma_f32_16x16x32_f16 v[54:57], v[156:159], v[140:143], v[54:57]
	ds_read_b128 v[128:131], v93 offset:6144
	v_mfma_f32_16x16x32_f16 v[50:53], v[160:163], v[140:143], v[50:53]
	ds_read_b128 v[112:115], v91 offset:6144
	v_mfma_f32_16x16x32_f16 v[46:49], v[164:167], v[140:143], v[46:49]
	ds_read_b128 v[132:135], v93 offset:8192
	v_mfma_f32_16x16x32_f16 v[42:45], v[168:171], v[140:143], v[42:45]
	v_mfma_f32_16x16x32_f16 v[38:41], v[152:155], v[144:147], v[38:41]
	global_load_lds_dwordx4 v82, s[22:23]
	s_add_u32 m0, m0, 0x2000
	v_mfma_f32_16x16x32_f16 v[30:33], v[156:159], v[144:147], v[30:33]
	v_mfma_f32_16x16x32_f16 v[26:29], v[160:163], v[144:147], v[26:29]
	v_mfma_f32_16x16x32_f16 v[22:25], v[164:167], v[144:147], v[22:25]
	global_load_lds_dwordx4 v83, s[22:23]
	s_add_u32 m0, m0, 0x2000
	v_mfma_f32_16x16x32_f16 v[18:21], v[168:171], v[144:147], v[18:21]
	v_mfma_f32_16x16x32_f16 v[14:17], v[152:155], v[148:151], v[14:17]
	v_mfma_f32_16x16x32_f16 v[10:13], v[156:159], v[148:151], v[10:13]
	global_load_lds_dwordx4 v84, s[22:23]
	s_add_u32 m0, m0, 0x2000
	v_mfma_f32_16x16x32_f16 v[2:5], v[160:163], v[148:151], v[2:5]
	v_mfma_f32_16x16x32_f16 v[6:9], v[164:167], v[148:151], v[6:9]
	v_mfma_f32_16x16x32_f16 v[66:69], v[168:171], v[148:151], v[66:69]
	global_load_lds_dwordx4 v85, s[22:23]
	s_add_u32 m0, m0, 0x2000
	s_mov_b32 s17, s27
	s_add_i32 s16, s16, 1
	s_cmp_lt_u32 s16, 13
	s_cbranch_scc1 .Lg1_loop
	s_add_i32 s27, s17, 0xd000
	s_cmp_lg_u32 s27, 0x27000
	s_cselect_b32 s27, s27, 0
	s_waitcnt lgkmcnt(0)
	v_mfma_f32_16x16x32_f16 v[34:37], v[116:119], v[100:103], v[34:37]
	ds_read_b128 v[152:155], v94
	v_mfma_f32_16x16x32_f16 v[78:81], v[120:123], v[100:103], v[78:81]
	ds_read_b128 v[136:139], v92
	v_mfma_f32_16x16x32_f16 v[74:77], v[124:127], v[100:103], v[74:77]
	ds_read_b128 v[156:159], v94 offset:2048
	v_mfma_f32_16x16x32_f16 v[70:73], v[128:131], v[100:103], v[70:73]
	ds_read_b128 v[140:143], v92 offset:2048
	v_mfma_f32_16x16x32_f16 v[62:65], v[132:135], v[100:103], v[62:65]
	ds_read_b128 v[160:163], v94 offset:4096
	v_mfma_f32_16x16x32_f16 v[58:61], v[116:119], v[104:107], v[58:61]
	ds_read_b128 v[144:147], v92 offset:4096
	v_mfma_f32_16x16x32_f16 v[54:57], v[120:123], v[104:107], v[54:57]
	ds_read_b128 v[164:167], v94 offset:6144
	v_mfma_f32_16x16x32_f16 v[50:53], v[124:127], v[104:107], v[50:53]
	ds_read_b128 v[148:151], v92 offset:6144
	v_mfma_f32_16x16x32_f16 v[46:49], v[128:131], v[104:107], v[46:49]
	ds_read_b128 v[168:171], v94 offset:8192
	v_mfma_f32_16x16x32_f16 v[42:45], v[132:135], v[104:107], v[42:45]
	v_mfma_f32_16x16x32_f16 v[38:41], v[116:119], v[108:111], v[38:41]
	v_add_u32_e32 v91, s27, v89
	v_mfma_f32_16x16x32_f16 v[30:33], v[120:123], v[108:111], v[30:33]
	v_add_u32_e32 v93, s27, v90
	v_mfma_f32_16x16x32_f16 v[26:29], v[124:127], v[108:111], v[26:29]
	v_xor_b32_e32 v92, 64, v91
	v_mfma_f32_16x16x32_f16 v[22:25], v[128:131], v[108:111], v[22:25]
	v_xor_b32_e32 v94, 64, v93
	v_mfma_f32_16x16x32_f16 v[18:21], v[132:135], v[108:111], v[18:21]
	global_load_lds_dwordx4 v86, s[24:25]
	s_add_u32 m0, m0, 0x2000
	v_mfma_f32_16x16x32_f16 v[14:17], v[116:119], v[112:115], v[14:17]
	v_mfma_f32_16x16x32_f16 v[10:13], v[120:123], v[112:115], v[10:13]
	global_load_lds_dwordx4 v87, s[24:25]
	s_mov_b32 m0, s30
	v_mfma_f32_16x16x32_f16 v[2:5], v[124:127], v[112:115], v[2:5]
	v_mfma_f32_16x16x32_f16 v[6:9], v[128:131], v[112:115], v[6:9]
	global_load_lds_dwordx4 v88, s[24:25]
	v_mfma_f32_16x16x32_f16 v[66:69], v[132:135], v[112:115], v[66:69]
	s_waitcnt vmcnt(7)
	s_waitcnt lgkmcnt(0)
	s_barrier
	v_mfma_f32_16x16x32_f16 v[34:37], v[152:155], v[136:139], v[34:37]
	ds_read_b128 v[116:119], v93
	v_mfma_f32_16x16x32_f16 v[78:81], v[156:159], v[136:139], v[78:81]
	ds_read_b128 v[100:103], v91
	v_mfma_f32_16x16x32_f16 v[74:77], v[160:163], v[136:139], v[74:77]
	ds_read_b128 v[120:123], v93 offset:2048
	v_mfma_f32_16x16x32_f16 v[70:73], v[164:167], v[136:139], v[70:73]
	ds_read_b128 v[104:107], v91 offset:2048
	v_mfma_f32_16x16x32_f16 v[62:65], v[168:171], v[136:139], v[62:65]
	ds_read_b128 v[124:127], v93 offset:4096
	v_mfma_f32_16x16x32_f16 v[58:61], v[152:155], v[140:143], v[58:61]
	ds_read_b128 v[108:111], v91 offset:4096
	v_mfma_f32_16x16x32_f16 v[54:57], v[156:159], v[140:143], v[54:57]
	ds_read_b128 v[128:131], v93 offset:6144
	v_mfma_f32_16x16x32_f16 v[50:53], v[160:163], v[140:143], v[50:53]
	ds_read_b128 v[112:115], v91 offset:6144
	v_mfma_f32_16x16x32_f16 v[46:49], v[164:167], v[140:143], v[46:49]
	ds_read_b128 v[132:135], v93 offset:8192
	v_mfma_f32_16x16x32_f16 v[42:45], v[168:171], v[140:143], v[42:45]
	v_mfma_f32_16x16x32_f16 v[38:41], v[152:155], v[144:147], v[38:41]
	v_mfma_f32_16x16x32_f16 v[30:33], v[156:159], v[144:147], v[30:33]
	v_mfma_f32_16x16x32_f16 v[26:29], v[160:163], v[144:147], v[26:29]
	v_mfma_f32_16x16x32_f16 v[22:25], v[164:167], v[144:147], v[22:25]
	v_mfma_f32_16x16x32_f16 v[18:21], v[168:171], v[144:147], v[18:21]
	v_mfma_f32_16x16x32_f16 v[14:17], v[152:155], v[148:151], v[14:17]
	v_mfma_f32_16x16x32_f16 v[10:13], v[156:159], v[148:151], v[10:13]
	v_mfma_f32_16x16x32_f16 v[2:5], v[160:163], v[148:151], v[2:5]
	v_mfma_f32_16x16x32_f16 v[6:9], v[164:167], v[148:151], v[6:9]
	v_mfma_f32_16x16x32_f16 v[66:69], v[168:171], v[148:151], v[66:69]
	s_mov_b32 s17, s27
	s_add_i32 s16, s16, 1
	s_add_i32 s27, s17, 0xd000
	s_cmp_lg_u32 s27, 0x27000
	s_cselect_b32 s27, s27, 0
	s_waitcnt lgkmcnt(0)
	v_mfma_f32_16x16x32_f16 v[34:37], v[116:119], v[100:103], v[34:37]
	ds_read_b128 v[152:155], v94
	v_mfma_f32_16x16x32_f16 v[78:81], v[120:123], v[100:103], v[78:81]
	ds_read_b128 v[136:139], v92
	v_mfma_f32_16x16x32_f16 v[74:77], v[124:127], v[100:103], v[74:77]
	ds_read_b128 v[156:159], v94 offset:2048
	v_mfma_f32_16x16x32_f16 v[70:73], v[128:131], v[100:103], v[70:73]
	ds_read_b128 v[140:143], v92 offset:2048
	v_mfma_f32_16x16x32_f16 v[62:65], v[132:135], v[100:103], v[62:65]
	ds_read_b128 v[160:163], v94 offset:4096
	v_mfma_f32_16x16x32_f16 v[58:61], v[116:119], v[104:107], v[58:61]
	ds_read_b128 v[144:147], v92 offset:4096
	v_mfma_f32_16x16x32_f16 v[54:57], v[120:123], v[104:107], v[54:57]
	ds_read_b128 v[164:167], v94 offset:6144
	v_mfma_f32_16x16x32_f16 v[50:53], v[124:127], v[104:107], v[50:53]
	ds_read_b128 v[148:151], v92 offset:6144
	v_mfma_f32_16x16x32_f16 v[46:49], v[128:131], v[104:107], v[46:49]
	ds_read_b128 v[168:171], v94 offset:8192
	v_mfma_f32_16x16x32_f16 v[42:45], v[132:135], v[104:107], v[42:45]
	v_mfma_f32_16x16x32_f16 v[38:41], v[116:119], v[108:111], v[38:41]
	v_add_u32_e32 v91, s27, v89
	v_mfma_f32_16x16x32_f16 v[30:33], v[120:123], v[108:111], v[30:33]
	v_add_u32_e32 v93, s27, v90
	v_mfma_f32_16x16x32_f16 v[26:29], v[124:127], v[108:111], v[26:29]
	v_xor_b32_e32 v92, 64, v91
	v_mfma_f32_16x16x32_f16 v[22:25], v[128:131], v[108:111], v[22:25]
	v_xor_b32_e32 v94, 64, v93
	v_mfma_f32_16x16x32_f16 v[18:21], v[132:135], v[108:111], v[18:21]
	v_mfma_f32_16x16x32_f16 v[14:17], v[116:119], v[112:115], v[14:17]
	v_mfma_f32_16x16x32_f16 v[10:13], v[120:123], v[112:115], v[10:13]
	v_mfma_f32_16x16x32_f16 v[2:5], v[124:127], v[112:115], v[2:5]
	v_mfma_f32_16x16x32_f16 v[6:9], v[128:131], v[112:115], v[6:9]
	v_mfma_f32_16x16x32_f16 v[66:69], v[132:135], v[112:115], v[66:69]
	s_waitcnt vmcnt(0)
	s_waitcnt lgkmcnt(0)
	s_barrier
	v_mfma_f32_16x16x32_f16 v[34:37], v[152:155], v[136:139], v[34:37]
	ds_read_b128 v[116:119], v93
	v_mfma_f32_16x16x32_f16 v[78:81], v[156:159], v[136:139], v[78:81]
	ds_read_b128 v[100:103], v91
	v_mfma_f32_16x16x32_f16 v[74:77], v[160:163], v[136:139], v[74:77]
	ds_read_b128 v[120:123], v93 offset:2048
	v_mfma_f32_16x16x32_f16 v[70:73], v[164:167], v[136:139], v[70:73]
	ds_read_b128 v[104:107], v91 offset:2048
	v_mfma_f32_16x16x32_f16 v[62:65], v[168:171], v[136:139], v[62:65]
	ds_read_b128 v[124:127], v93 offset:4096
	v_mfma_f32_16x16x32_f16 v[58:61], v[152:155], v[140:143], v[58:61]
	ds_read_b128 v[108:111], v91 offset:4096
	v_mfma_f32_16x16x32_f16 v[54:57], v[156:159], v[140:143], v[54:57]
	ds_read_b128 v[128:131], v93 offset:6144
	v_mfma_f32_16x16x32_f16 v[50:53], v[160:163], v[140:143], v[50:53]
	ds_read_b128 v[112:115], v91 offset:6144
	v_mfma_f32_16x16x32_f16 v[46:49], v[164:167], v[140:143], v[46:49]
	ds_read_b128 v[132:135], v93 offset:8192
	v_mfma_f32_16x16x32_f16 v[42:45], v[168:171], v[140:143], v[42:45]
	v_mfma_f32_16x16x32_f16 v[38:41], v[152:155], v[144:147], v[38:41]
	v_mfma_f32_16x16x32_f16 v[30:33], v[156:159], v[144:147], v[30:33]
	v_mfma_f32_16x16x32_f16 v[26:29], v[160:163], v[144:147], v[26:29]
	v_mfma_f32_16x16x32_f16 v[22:25], v[164:167], v[144:147], v[22:25]
	v_mfma_f32_16x16x32_f16 v[18:21], v[168:171], v[144:147], v[18:21]
	v_mfma_f32_16x16x32_f16 v[14:17], v[152:155], v[148:151], v[14:17]
	v_mfma_f32_16x16x32_f16 v[10:13], v[156:159], v[148:151], v[10:13]
	v_mfma_f32_16x16x32_f16 v[2:5], v[160:163], v[148:151], v[2:5]
	v_mfma_f32_16x16x32_f16 v[6:9], v[164:167], v[148:151], v[6:9]
	v_mfma_f32_16x16x32_f16 v[66:69], v[168:171], v[148:151], v[66:69]
	s_mov_b32 s17, s27
	s_add_i32 s16, s16, 1
	s_add_i32 s27, s17, 0xd000
	s_cmp_lg_u32 s27, 0x27000
	s_cselect_b32 s27, s27, 0
	s_waitcnt lgkmcnt(0)
	v_mfma_f32_16x16x32_f16 v[34:37], v[116:119], v[100:103], v[34:37]
	ds_read_b128 v[152:155], v94
	v_mfma_f32_16x16x32_f16 v[78:81], v[120:123], v[100:103], v[78:81]
	ds_read_b128 v[136:139], v92
	v_mfma_f32_16x16x32_f16 v[74:77], v[124:127], v[100:103], v[74:77]
	ds_read_b128 v[156:159], v94 offset:2048
	v_mfma_f32_16x16x32_f16 v[70:73], v[128:131], v[100:103], v[70:73]
	ds_read_b128 v[140:143], v92 offset:2048
	v_mfma_f32_16x16x32_f16 v[62:65], v[132:135], v[100:103], v[62:65]
	ds_read_b128 v[160:163], v94 offset:4096
	v_mfma_f32_16x16x32_f16 v[58:61], v[116:119], v[104:107], v[58:61]
	ds_read_b128 v[144:147], v92 offset:4096
	v_mfma_f32_16x16x32_f16 v[54:57], v[120:123], v[104:107], v[54:57]
	ds_read_b128 v[164:167], v94 offset:6144
	v_mfma_f32_16x16x32_f16 v[50:53], v[124:127], v[104:107], v[50:53]
	ds_read_b128 v[148:151], v92 offset:6144
	v_mfma_f32_16x16x32_f16 v[46:49], v[128:131], v[104:107], v[46:49]
	ds_read_b128 v[168:171], v94 offset:8192
	v_mfma_f32_16x16x32_f16 v[42:45], v[132:135], v[104:107], v[42:45]
	v_mfma_f32_16x16x32_f16 v[38:41], v[116:119], v[108:111], v[38:41]
	v_add_u32_e32 v91, s27, v89
	v_mfma_f32_16x16x32_f16 v[30:33], v[120:123], v[108:111], v[30:33]
	v_add_u32_e32 v93, s27, v90
	v_mfma_f32_16x16x32_f16 v[26:29], v[124:127], v[108:111], v[26:29]
	v_xor_b32_e32 v92, 64, v91
	v_mfma_f32_16x16x32_f16 v[22:25], v[128:131], v[108:111], v[22:25]
	v_xor_b32_e32 v94, 64, v93
	v_mfma_f32_16x16x32_f16 v[18:21], v[132:135], v[108:111], v[18:21]
	v_mfma_f32_16x16x32_f16 v[14:17], v[116:119], v[112:115], v[14:17]
	v_mfma_f32_16x16x32_f16 v[10:13], v[120:123], v[112:115], v[10:13]
	v_mfma_f32_16x16x32_f16 v[2:5], v[124:127], v[112:115], v[2:5]
	v_mfma_f32_16x16x32_f16 v[6:9], v[128:131], v[112:115], v[6:9]
	v_mfma_f32_16x16x32_f16 v[66:69], v[132:135], v[112:115], v[66:69]
	s_waitcnt lgkmcnt(0)
	s_barrier
	v_mfma_f32_16x16x32_f16 v[34:37], v[152:155], v[136:139], v[34:37]
	ds_read_b128 v[116:119], v93
	v_mfma_f32_16x16x32_f16 v[78:81], v[156:159], v[136:139], v[78:81]
	ds_read_b128 v[100:103], v91
	v_mfma_f32_16x16x32_f16 v[74:77], v[160:163], v[136:139], v[74:77]
	ds_read_b128 v[120:123], v93 offset:2048
	v_mfma_f32_16x16x32_f16 v[70:73], v[164:167], v[136:139], v[70:73]
	ds_read_b128 v[104:107], v91 offset:2048
	v_mfma_f32_16x16x32_f16 v[62:65], v[168:171], v[136:139], v[62:65]
	ds_read_b128 v[124:127], v93 offset:4096
	v_mfma_f32_16x16x32_f16 v[58:61], v[152:155], v[140:143], v[58:61]
	ds_read_b128 v[108:111], v91 offset:4096
	v_mfma_f32_16x16x32_f16 v[54:57], v[156:159], v[140:143], v[54:57]
	ds_read_b128 v[128:131], v93 offset:6144
	v_mfma_f32_16x16x32_f16 v[50:53], v[160:163], v[140:143], v[50:53]
	ds_read_b128 v[112:115], v91 offset:6144
	v_mfma_f32_16x16x32_f16 v[46:49], v[164:167], v[140:143], v[46:49]
	ds_read_b128 v[132:135], v93 offset:8192
	v_mfma_f32_16x16x32_f16 v[42:45], v[168:171], v[140:143], v[42:45]
	v_mfma_f32_16x16x32_f16 v[38:41], v[152:155], v[144:147], v[38:41]
	v_mfma_f32_16x16x32_f16 v[30:33], v[156:159], v[144:147], v[30:33]
	v_mfma_f32_16x16x32_f16 v[26:29], v[160:163], v[144:147], v[26:29]
	v_mfma_f32_16x16x32_f16 v[22:25], v[164:167], v[144:147], v[22:25]
	v_mfma_f32_16x16x32_f16 v[18:21], v[168:171], v[144:147], v[18:21]
	v_mfma_f32_16x16x32_f16 v[14:17], v[152:155], v[148:151], v[14:17]
	v_mfma_f32_16x16x32_f16 v[10:13], v[156:159], v[148:151], v[10:13]
	v_mfma_f32_16x16x32_f16 v[2:5], v[160:163], v[148:151], v[2:5]
	v_mfma_f32_16x16x32_f16 v[6:9], v[164:167], v[148:151], v[6:9]
	v_mfma_f32_16x16x32_f16 v[66:69], v[168:171], v[148:151], v[66:69]
	s_mov_b32 s17, s27
	s_add_i32 s16, s16, 1
	s_nop 7

.Lg1_pad_exit:
	s_endpgm
	.p2alignl 8, 3212836864

_Z8gemm_f16ILi128ELi64ELi2ELi2ELi4ELi2ELi0EEvPKDF16_S1_Pviiii:
	s_load_dwordx4 s[4:7], s[0:1], 0x0
	s_load_dwordx2 s[8:9], s[0:1], 0x10
	s_and_b32 s3, s2, 7
	s_lshr_b32 s10, s2, 3
	s_lshr_b32 s11, s3, 1
	s_lshl_b32 s11, s11, 2
	s_and_b32 s12, s10, 3
	s_and_b32 s3, s3, 1
	s_lshl_b32 s3, s3, 3
	s_lshr_b32 s10, s10, 2
	s_add_i32 s10, s10, s3
	s_add_i32 s3, s11, s12
	s_mov_b32 s11, s10
	s_lshl_b32 s10, s3, 7
	s_lshl_b32 s11, s11, 6
	v_lshrrev_b32_e32 v13, 3, v0
	v_and_b32_e32 v14, 7, v0
	v_bfe_u32 v15, v0, 4, 3
	v_xor_b32_e32 v14, v14, v15
	v_lshlrev_b32_e32 v14, 4, v14
	v_add_u32_e32 v15, s10, v13
	v_mul_u32_u24_e32 v15, 0xc00, v15
	v_add_u32_e32 v3, v15, v14
	v_add_u32_e32 v4, 0x18000, v3
	v_add_u32_e32 v5, 0x30000, v3
	v_add_u32_e32 v6, 0x48000, v3
	v_add_u32_e32 v15, s11, v13
	v_mul_u32_u24_e32 v15, 0xc00, v15
	v_add_u32_e32 v7, v15, v14
	v_add_u32_e32 v8, 0x18000, v7
	v_lshlrev_b32_e32 v13, 4, v0
	s_nop 0
	v_readfirstlane_b32 s20, v13
	v_and_b32_e32 v13, 15, v0
	v_bfe_u32 v14, v0, 4, 2
	v_bfe_u32 v15, v0, 1, 3
	v_xor_b32_e32 v14, v14, v15
	v_lshlrev_b32_e32 v14, 4, v14
	v_lshl_or_b32 v14, v13, 7, v14
	v_lshrrev_b32_e32 v13, 7, v0
	v_lshl_or_b32 v1, v13, 13, v14
	v_bfe_u32 v13, v0, 6, 1
	v_lshlrev_b32_e32 v13, 12, v13
	v_or_b32_e32 v13, 0x4000, v13
	v_or_b32_e32 v2, v13, v14
	s_waitcnt lgkmcnt(0)
	s_mov_b32 s14, s4
	s_mov_b32 s15, s5
	s_mov_b32 s16, s6
	s_mov_b32 s17, s7
	s_mov_b32 s21, s20
	s_mov_b32 m0, s21
	s_add_i32 s21, s21, 0x1000
	global_load_lds_dwordx4 v3, s[14:15]
	s_mov_b32 m0, s21
	s_add_i32 s21, s21, 0x1000
	global_load_lds_dwordx4 v4, s[14:15]
	s_mov_b32 m0, s21
	s_add_i32 s21, s21, 0x1000
	global_load_lds_dwordx4 v5, s[14:15]
	s_mov_b32 m0, s21
	s_add_i32 s21, s21, 0x1000
	global_load_lds_dwordx4 v6, s[14:15]
	s_mov_b32 m0, s21
	s_add_i32 s21, s21, 0x1000
	global_load_lds_dwordx4 v7, s[16:17]
	s_mov_b32 m0, s21
	s_add_i32 s21, s21, 0x1000
	global_load_lds_dwordx4 v8, s[16:17]
	s_add_u32 s14, s14, 0x80
	s_addc_u32 s15, s15, 0
	s_add_u32 s16, s16, 0x80
	s_addc_u32 s17, s17, 0
	s_mov_b32 m0, s21
	s_add_i32 s21, s21, 0x1000
	global_load_lds_dwordx4 v3, s[14:15]
	s_mov_b32 m0, s21
	s_add_i32 s21, s21, 0x1000
	global_load_lds_dwordx4 v4, s[14:15]
	s_mov_b32 m0, s21
	s_add_i32 s21, s21, 0x1000
	global_load_lds_dwordx4 v5, s[14:15]
	s_mov_b32 m0, s21
	s_add_i32 s21, s21, 0x1000
	global_load_lds_dwordx4 v6, s[14:15]
	s_mov_b32 m0, s21
	s_add_i32 s21, s21, 0x1000
	global_load_lds_dwordx4 v7, s[16:17]
	s_mov_b32 m0, s21
	s_add_i32 s21, s21, 0x1000
	global_load_lds_dwordx4 v8, s[16:17]
	s_add_u32 s14, s14, 0x80
	s_addc_u32 s15, s15, 0
	s_add_u32 s16, s16, 0x80
	s_addc_u32 s17, s17, 0
	s_mov_b32 m0, s21
	s_add_i32 s21, s21, 0x1000
	global_load_lds_dwordx4 v3, s[14:15]
	s_mov_b32 m0, s21
	s_add_i32 s21, s21, 0x1000
	global_load_lds_dwordx4 v4, s[14:15]
	s_mov_b32 m0, s21
	s_add_i32 s21, s21, 0x1000
	global_load_lds_dwordx4 v5, s[14:15]
	s_mov_b32 m0, s21
	s_add_i32 s21, s21, 0x1000
	global_load_lds_dwordx4 v6, s[14:15]
	s_mov_b32 m0, s21
	s_add_i32 s21, s21, 0x1000
	global_load_lds_dwordx4 v7, s[16:17]
	s_mov_b32 m0, s21
	s_add_i32 s21, s21, 0x1000
	global_load_lds_dwordx4 v8, s[16:17]
	s_add_u32 s14, s14, 0x80
	s_addc_u32 s15, s15, 0
	s_add_u32 s16, s16, 0x80
	s_addc_u32 s17, s17, 0
	s_mov_b32 m0, s21
	s_add_i32 s21, s21, 0x1000
	global_load_lds_dwordx4 v3, s[14:15]
	s_mov_b32 m0, s21
	s_add_i32 s21, s21, 0x1000
	global_load_lds_dwordx4 v4, s[14:15]
	s_mov_b32 m0, s21
	s_add_i32 s21, s21, 0x1000
	global_load_lds_dwordx4 v5, s[14:15]
	s_mov_b32 m0, s21
	s_add_i32 s21, s21, 0x1000
	global_load_lds_dwordx4 v6, s[14:15]
	s_mov_b32 m0, s21
	s_add_i32 s21, s21, 0x1000
	global_load_lds_dwordx4 v7, s[16:17]
	s_mov_b32 m0, s21
	s_add_i32 s21, s21, 0x1000
	global_load_lds_dwordx4 v8, s[16:17]
	v_accvgpr_write_b32 a0, 0
	v_accvgpr_write_b32 a1, 0
	v_accvgpr_write_b32 a2, 0
	v_accvgpr_write_b32 a3, 0
	v_accvgpr_write_b32 a4, 0
	v_accvgpr_write_b32 a5, 0
	v_accvgpr_write_b32 a6, 0
	v_accvgpr_write_b32 a7, 0
	v_accvgpr_write_b32 a8, 0
	v_accvgpr_write_b32 a9, 0
	v_accvgpr_write_b32 a10, 0
	v_accvgpr_write_b32 a11, 0
	v_accvgpr_write_b32 a12, 0
	v_accvgpr_write_b32 a13, 0
	v_accvgpr_write_b32 a14, 0
	v_accvgpr_write_b32 a15, 0
	v_accvgpr_write_b32 a16, 0
	v_accvgpr_write_b32 a17, 0
	v_accvgpr_write_b32 a18, 0
	v_accvgpr_write_b32 a19, 0
	v_accvgpr_write_b32 a20, 0
	v_accvgpr_write_b32 a21, 0
	v_accvgpr_write_b32 a22, 0
	v_accvgpr_write_b32 a23, 0
	v_accvgpr_write_b32 a24, 0
	v_accvgpr_write_b32 a25, 0
	v_accvgpr_write_b32 a26, 0
	v_accvgpr_write_b32 a27, 0
	v_accvgpr_write_b32 a28, 0
	v_accvgpr_write_b32 a29, 0
	v_accvgpr_write_b32 a30, 0
	v_accvgpr_write_b32 a31, 0
	s_mov_b32 s12, 0
	s_mov_b32 s13, 0
	v_mov_b32_e32 v9, v1
	v_mov_b32_e32 v11, v2
	v_xor_b32_e32 v10, 64, v1
	v_xor_b32_e32 v12, 64, v2
	s_waitcnt vmcnt(18)
	s_barrier
	ds_read_b128 v[16:19], v11
	ds_read_b128 v[24:27], v9
	ds_read_b128 v[20:23], v11 offset:2048
	ds_read_b128 v[28:31], v9 offset:2048
	ds_read_b128 v[32:35], v9 offset:4096
	ds_read_b128 v[36:39], v9 offset:6144
	s_add_i32 s23, s13, 0x6000
	s_cmp_lg_u32 s23, 0x18000
	s_cselect_b32 s23, s23, 0
	s_waitcnt lgkmcnt(0)
	v_mfma_f32_16x16x32_f16 a[0:3], v[16:19], v[24:27], a[0:3]
	ds_read_b128 v[40:43], v12
	v_mfma_f32_16x16x32_f16 a[4:7], v[20:23], v[24:27], a[4:7]
	ds_read_b128 v[48:51], v10
	v_mfma_f32_16x16x32_f16 a[8:11], v[16:19], v[28:31], a[8:11]
	ds_read_b128 v[44:47], v12 offset:2048
	v_mfma_f32_16x16x32_f16 a[12:15], v[20:23], v[28:31], a[12:15]
	ds_read_b128 v[52:55], v10 offset:2048
	v_mfma_f32_16x16x32_f16 a[16:19], v[16:19], v[32:35], a[16:19]
	ds_read_b128 v[56:59], v10 offset:4096
	v_mfma_f32_16x16x32_f16 a[20:23], v[20:23], v[32:35], a[20:23]
	ds_read_b128 v[60:63], v10 offset:6144
	v_mfma_f32_16x16x32_f16 a[24:27], v[16:19], v[36:39], a[24:27]
	v_add_u32_e32 v9, s23, v1
	v_add_u32_e32 v11, s23, v2
	v_mfma_f32_16x16x32_f16 a[28:31], v[20:23], v[36:39], a[28:31]
	v_xor_b32_e32 v10, 64, v9
	v_xor_b32_e32 v12, 64, v11
	s_add_i32 s22, s12, 4
	s_lshl_b32 s22, s22, 7
	s_add_u32 s14, s4, s22
	s_addc_u32 s15, s5, 0
	s_add_u32 s16, s6, s22
	s_addc_u32 s17, s7, 0
	s_add_i32 s21, s13, s20
	s_waitcnt vmcnt(12)
	s_waitcnt lgkmcnt(0)
	s_barrier
	s_mov_b32 m0, s21
	v_mfma_f32_16x16x32_f16 a[0:3], v[40:43], v[48:51], a[0:3]
	ds_read_b128 v[16:19], v11
	v_mfma_f32_16x16x32_f16 a[4:7], v[44:47], v[48:51], a[4:7]
	ds_read_b128 v[24:27], v9
	global_load_lds_dwordx4 v3, s[14:15]
	s_add_u32 m0, m0, 0x1000
	v_mfma_f32_16x16x32_f16 a[8:11], v[40:43], v[52:55], a[8:11]
	ds_read_b128 v[20:23], v11 offset:2048
	v_mfma_f32_16x16x32_f16 a[12:15], v[44:47], v[52:55], a[12:15]
	ds_read_b128 v[28:31], v9 offset:2048
	global_load_lds_dwordx4 v4, s[14:15]
	s_add_u32 m0, m0, 0x1000
	v_mfma_f32_16x16x32_f16 a[16:19], v[40:43], v[56:59], a[16:19]
	ds_read_b128 v[32:35], v9 offset:4096
	v_mfma_f32_16x16x32_f16 a[20:23], v[44:47], v[56:59], a[20:23]
	ds_read_b128 v[36:39], v9 offset:6144
	global_load_lds_dwordx4 v5, s[14:15]
	s_add_u32 m0, m0, 0x1000
	v_mfma_f32_16x16x32_f16 a[24:27], v[40:43], v[60:63], a[24:27]
	v_mfma_f32_16x16x32_f16 a[28:31], v[44:47], v[60:63], a[28:31]
	global_load_lds_dwordx4 v6, s[14:15]
	s_add_u32 m0, m0, 0x1000
	s_mov_b32 s13, s23
	s_add_i32 s12, s12, 1
.Lg2_loop:
	s_add_i32 s23, s13, 0x6000
	s_cmp_lg_u32 s23, 0x18000
	s_cselect_b32 s23, s23, 0
	s_waitcnt lgkmcnt(0)
	v_mfma_f32_16x16x32_f16 a[0:3], v[16:19], v[24:27], a[0:3]
	ds_read_b128 v[40:43], v12
	v_mfma_f32_16x16x32_f16 a[4:7], v[20:23], v[24:27], a[4:7]
	ds_read_b128 v[48:51], v10
	v_mfma_f32_16x16x32_f16 a[8:11], v[16:19], v[28:31], a[8:11]
	ds_read_b128 v[44:47], v12 offset:2048
	v_mfma_f32_16x16x32_f16 a[12:15], v[20:23], v[28:31], a[12:15]
	ds_read_b128 v[52:55], v10 offset:2048
	global_load_lds_dwordx4 v7, s[16:17]
	s_add_u32 m0, m0, 0x1000
	v_mfma_f32_16x16x32_f16 a[16:19], v[16:19], v[32:35], a[16:19]
	ds_read_b128 v[56:59], v10 offset:4096
	v_mfma_f32_16x16x32_f16 a[20:23], v[20:23], v[32:35], a[20:23]
	ds_read_b128 v[60:63], v10 offset:6144
	v_mfma_f32_16x16x32_f16 a[24:27], v[16:19], v[36:39], a[24:27]
	v_add_u32_e32 v9, s23, v1
	v_add_u32_e32 v11, s23, v2
	global_load_lds_dwordx4 v8, s[16:17]
	v_mfma_f32_16x16x32_f16 a[28:31], v[20:23], v[36:39], a[28:31]
	v_xor_b32_e32 v10, 64, v9
	v_xor_b32_e32 v12, 64, v11
	s_add_i32 s22, s12, 4
	s_lshl_b32 s22, s22, 7
	s_add_u32 s14, s4, s22
	s_addc_u32 s15, s5, 0
	s_add_u32 s16, s6, s22
	s_addc_u32 s17, s7, 0
	s_add_i32 s21, s13, s20
	s_waitcnt vmcnt(12)
	s_waitcnt lgkmcnt(0)
	s_barrier
	s_mov_b32 m0, s21
	v_mfma_f32_16x16x32_f16 a[0:3], v[40:43], v[48:51], a[0:3]
	ds_read_b128 v[16:19], v11
	v_mfma_f32_16x16x32_f16 a[4:7], v[44:47], v[48:51], a[4:7]
	ds_read_b128 v[24:27], v9
	global_load_lds_dwordx4 v3, s[14:15]
	s_add_u32 m0, m0, 0x1000
	v_mfma_f32_16x16x32_f16 a[8:11], v[40:43], v[52:55], a[8:11]
	ds_read_b128 v[20:23], v11 offset:2048
	v_mfma_f32_16x16x32_f16 a[12:15], v[44:47], v[52:55], a[12:15]
	ds_read_b128 v[28:31], v9 offset:2048
	global_load_lds_dwordx4 v4, s[14:15]
	s_add_u32 m0, m0, 0x1000
	v_mfma_f32_16x16x32_f16 a[16:19], v[40:43], v[56:59], a[16:19]
	ds_read_b128 v[32:35], v9 offset:4096
	v_mfma_f32_16x16x32_f16 a[20:23], v[44:47], v[56:59], a[20:23]
	ds_read_b128 v[36:39], v9 offset:6144
	global_load_lds_dwordx4 v5, s[14:15]
	s_add_u32 m0, m0, 0x1000
	v_mfma_f32_16x16x32_f16 a[24:27], v[40:43], v[60:63], a[24:27]
	v_mfma_f32_16x16x32_f16 a[28:31], v[44:47], v[60:63], a[28:31]
	global_load_lds_dwordx4 v6, s[14:15]
	s_add_u32 m0, m0, 0x1000
	s_mov_b32 s13, s23
	s_add_i32 s12, s12, 1
	s_cmp_lt_u32 s12, 20
	s_cbranch_scc1 .Lg2_loop
	s_add_i32 s23, s13, 0x6000
	s_cmp_lg_u32 s23, 0x18000
	s_cselect_b32 s23, s23, 0
	s_waitcnt lgkmcnt(0)
	v_mfma_f32_16x16x32_f16 a[0:3], v[16:19], v[24:27], a[0:3]
	ds_read_b128 v[40:43], v12
	v_mfma_f32_16x16x32_f16 a[4:7], v[20:23], v[24:27], a[4:7]
	ds_read_b128 v[48:51], v10
	v_mfma_f32_16x16x32_f16 a[8:11], v[16:19], v[28:31], a[8:11]
	ds_read_b128 v[44:47], v12 offset:2048
	v_mfma_f32_16x16x32_f16 a[12:15], v[20:23], v[28:31], a[12:15]
	ds_read_b128 v[52:55], v10 offset:2048
	global_load_lds_dwordx4 v7, s[16:17]
	s_add_u32 m0, m0, 0x1000
	v_mfma_f32_16x16x32_f16 a[16:19], v[16:19], v[32:35], a[16:19]
	ds_read_b128 v[56:59], v10 offset:4096
	v_mfma_f32_16x16x32_f16 a[20:23], v[20:23], v[32:35], a[20:23]
	ds_read_b128 v[60:63], v10 offset:6144
	v_mfma_f32_16x16x32_f16 a[24:27], v[16:19], v[36:39], a[24:27]
	v_add_u32_e32 v9, s23, v1
	v_add_u32_e32 v11, s23, v2
	global_load_lds_dwordx4 v8, s[16:17]
	v_mfma_f32_16x16x32_f16 a[28:31], v[20:23], v[36:39], a[28:31]
	v_xor_b32_e32 v10, 64, v9
	v_xor_b32_e32 v12, 64, v11
	s_waitcnt vmcnt(12)
	s_waitcnt lgkmcnt(0)
	s_barrier
	v_mfma_f32_16x16x32_f16 a[0:3], v[40:43], v[48:51], a[0:3]
	ds_read_b128 v[16:19], v11
	v_mfma_f32_16x16x32_f16 a[4:7], v[44:47], v[48:51], a[4:7]
	ds_read_b128 v[24:27], v9
	v_mfma_f32_16x16x32_f16 a[8:11], v[40:43], v[52:55], a[8:11]
	ds_read_b128 v[20:23], v11 offset:2048
	v_mfma_f32_16x16x32_f16 a[12:15], v[44:47], v[52:55], a[12:15]
	ds_read_b128 v[28:31], v9 offset:2048
	v_mfma_f32_16x16x32_f16 a[16:19], v[40:43], v[56:59], a[16:19]
	ds_read_b128 v[32:35], v9 offset:4096
	v_mfma_f32_16x16x32_f16 a[20:23], v[44:47], v[56:59], a[20:23]
	ds_read_b128 v[36:39], v9 offset:6144
	v_mfma_f32_16x16x32_f16 a[24:27], v[40:43], v[60:63], a[24:27]
	v_mfma_f32_16x16x32_f16 a[28:31], v[44:47], v[60:63], a[28:31]
	s_mov_b32 s13, s23
	s_add_i32 s12, s12, 1
	s_add_i32 s23, s13, 0x6000
	s_cmp_lg_u32 s23, 0x18000
	s_cselect_b32 s23, s23, 0
	s_waitcnt lgkmcnt(0)
	v_mfma_f32_16x16x32_f16 a[0:3], v[16:19], v[24:27], a[0:3]
	ds_read_b128 v[40:43], v12
	v_mfma_f32_16x16x32_f16 a[4:7], v[20:23], v[24:27], a[4:7]
	ds_read_b128 v[48:51], v10
	v_mfma_f32_16x16x32_f16 a[8:11], v[16:19], v[28:31], a[8:11]
	ds_read_b128 v[44:47], v12 offset:2048
	v_mfma_f32_16x16x32_f16 a[12:15], v[20:23], v[28:31], a[12:15]
	ds_read_b128 v[52:55], v10 offset:2048
	v_mfma_f32_16x16x32_f16 a[16:19], v[16:19], v[32:35], a[16:19]
	ds_read_b128 v[56:59], v10 offset:4096
	v_mfma_f32_16x16x32_f16 a[20:23], v[20:23], v[32:35], a[20:23]
	ds_read_b128 v[60:63], v10 offset:6144
	v_mfma_f32_16x16x32_f16 a[24:27], v[16:19], v[36:39], a[24:27]
	v_add_u32_e32 v9, s23, v1
	v_add_u32_e32 v11, s23, v2
	v_mfma_f32_16x16x32_f16 a[28:31], v[20:23], v[36:39], a[28:31]
	v_xor_b32_e32 v10, 64, v9
	v_xor_b32_e32 v12, 64, v11
	s_waitcnt vmcnt(6)
	s_waitcnt lgkmcnt(0)
	s_barrier
	v_mfma_f32_16x16x32_f16 a[0:3], v[40:43], v[48:51], a[0:3]
	ds_read_b128 v[16:19], v11
	v_mfma_f32_16x16x32_f16 a[4:7], v[44:47], v[48:51], a[4:7]
	ds_read_b128 v[24:27], v9
	v_mfma_f32_16x16x32_f16 a[8:11], v[40:43], v[52:55], a[8:11]
	ds_read_b128 v[20:23], v11 offset:2048
	v_mfma_f32_16x16x32_f16 a[12:15], v[44:47], v[52:55], a[12:15]
	ds_read_b128 v[28:31], v9 offset:2048
	v_mfma_f32_16x16x32_f16 a[16:19], v[40:43], v[56:59], a[16:19]
	ds_read_b128 v[32:35], v9 offset:4096
	v_mfma_f32_16x16x32_f16 a[20:23], v[44:47], v[56:59], a[20:23]
	ds_read_b128 v[36:39], v9 offset:6144
	v_mfma_f32_16x16x32_f16 a[24:27], v[40:43], v[60:63], a[24:27]
	v_mfma_f32_16x16x32_f16 a[28:31], v[44:47], v[60:63], a[28:31]
	s_mov_b32 s13, s23
	s_add_i32 s12, s12, 1
	s_add_i32 s23, s13, 0x6000
	s_cmp_lg_u32 s23, 0x18000
	s_cselect_b32 s23, s23, 0
	s_waitcnt lgkmcnt(0)
	v_mfma_f32_16x16x32_f16 a[0:3], v[16:19], v[24:27], a[0:3]
	ds_read_b128 v[40:43], v12
	v_mfma_f32_16x16x32_f16 a[4:7], v[20:23], v[24:27], a[4:7]
	ds_read_b128 v[48:51], v10
	v_mfma_f32_16x16x32_f16 a[8:11], v[16:19], v[28:31], a[8:11]
	ds_read_b128 v[44:47], v12 offset:2048
	v_mfma_f32_16x16x32_f16 a[12:15], v[20:23], v[28:31], a[12:15]
	ds_read_b128 v[52:55], v10 offset:2048
	v_mfma_f32_16x16x32_f16 a[16:19], v[16:19], v[32:35], a[16:19]
	ds_read_b128 v[56:59], v10 offset:4096
	v_mfma_f32_16x16x32_f16 a[20:23], v[20:23], v[32:35], a[20:23]
	ds_read_b128 v[60:63], v10 offset:6144
	v_mfma_f32_16x16x32_f16 a[24:27], v[16:19], v[36:39], a[24:27]
	v_add_u32_e32 v9, s23, v1
	v_add_u32_e32 v11, s23, v2
	v_mfma_f32_16x16x32_f16 a[28:31], v[20:23], v[36:39], a[28:31]
	v_xor_b32_e32 v10, 64, v9
	v_xor_b32_e32 v12, 64, v11
	s_waitcnt vmcnt(0)
	s_waitcnt lgkmcnt(0)
	s_barrier
	v_mfma_f32_16x16x32_f16 a[0:3], v[40:43], v[48:51], a[0:3]
	ds_read_b128 v[16:19], v11
	v_mfma_f32_16x16x32_f16 a[4:7], v[44:47], v[48:51], a[4:7]
	ds_read_b128 v[24:27], v9
	v_mfma_f32_16x16x32_f16 a[8:11], v[40:43], v[52:55], a[8:11]
	ds_read_b128 v[20:23], v11 offset:2048
	v_mfma_f32_16x16x32_f16 a[12:15], v[44:47], v[52:55], a[12:15]
	ds_read_b128 v[28:31], v9 offset:2048
	v_mfma_f32_16x16x32_f16 a[16:19], v[40:43], v[56:59], a[16:19]
	ds_read_b128 v[32:35], v9 offset:4096
	v_mfma_f32_16x16x32_f16 a[20:23], v[44:47], v[56:59], a[20:23]
	ds_read_b128 v[36:39], v9 offset:6144
	v_mfma_f32_16x16x32_f16 a[24:27], v[40:43], v[60:63], a[24:27]
	v_mfma_f32_16x16x32_f16 a[28:31], v[44:47], v[60:63], a[28:31]
	s_mov_b32 s13, s23
	s_add_i32 s12, s12, 1
	s_add_i32 s23, s13, 0x6000
	s_cmp_lg_u32 s23, 0x18000
	s_cselect_b32 s23, s23, 0
	s_waitcnt lgkmcnt(0)
	v_mfma_f32_16x16x32_f16 a[0:3], v[16:19], v[24:27], a[0:3]
	ds_read_b128 v[40:43], v12
	v_mfma_f32_16x16x32_f16 a[4:7], v[20:23], v[24:27], a[4:7]
	ds_read_b128 v[48:51], v10
	v_mfma_f32_16x16x32_f16 a[8:11], v[16:19], v[28:31], a[8:11]
	ds_read_b128 v[44:47], v12 offset:2048
	v_mfma_f32_16x16x32_f16 a[12:15], v[20:23], v[28:31], a[12:15]
	ds_read_b128 v[52:55], v10 offset:2048
	v_mfma_f32_16x16x32_f16 a[16:19], v[16:19], v[32:35], a[16:19]
	ds_read_b128 v[56:59], v10 offset:4096
	v_mfma_f32_16x16x32_f16 a[20:23], v[20:23], v[32:35], a[20:23]
	ds_read_b128 v[60:63], v10 offset:6144
	v_mfma_f32_16x16x32_f16 a[24:27], v[16:19], v[36:39], a[24:27]
	v_add_u32_e32 v9, s23, v1
	v_add_u32_e32 v11, s23, v2
	v_mfma_f32_16x16x32_f16 a[28:31], v[20:23], v[36:39], a[28:31]
	v_xor_b32_e32 v10, 64, v9
	v_xor_b32_e32 v12, 64, v11
	s_waitcnt lgkmcnt(0)
	s_barrier
	v_mfma_f32_16x16x32_f16 a[0:3], v[40:43], v[48:51], a[0:3]
	ds_read_b128 v[16:19], v11
	v_mfma_f32_16x16x32_f16 a[4:7], v[44:47], v[48:51], a[4:7]
	ds_read_b128 v[24:27], v9
	v_mfma_f32_16x16x32_f16 a[8:11], v[40:43], v[52:55], a[8:11]
	ds_read_b128 v[20:23], v11 offset:2048
	v_mfma_f32_16x16x32_f16 a[12:15], v[44:47], v[52:55], a[12:15]
	ds_read_b128 v[28:31], v9 offset:2048
	v_mfma_f32_16x16x32_f16 a[16:19], v[40:43], v[56:59], a[16:19]
	ds_read_b128 v[32:35], v9 offset:4096
	v_mfma_f32_16x16x32_f16 a[20:23], v[44:47], v[56:59], a[20:23]
	ds_read_b128 v[36:39], v9 offset:6144
	v_mfma_f32_16x16x32_f16 a[24:27], v[40:43], v[60:63], a[24:27]
	v_mfma_f32_16x16x32_f16 a[28:31], v[44:47], v[60:63], a[28:31]
	s_mov_b32 s13, s23
	s_add_i32 s12, s12, 1
	s_waitcnt vmcnt(0) lgkmcnt(0)
	v_and_b32_e32 v13, 15, v0
	v_lshrrev_b32_e32 v14, 7, v0
	v_lshl_add_u32 v13, v14, 6, v13
	v_add_u32_e32 v13, s10, v13
	v_bfe_u32 v14, v0, 6, 1
	v_bfe_u32 v15, v0, 4, 2
	v_lshlrev_b32_e32 v14, 5, v14
	v_lshl_add_u32 v14, v15, 2, v14
	v_add_u32_e32 v14, s11, v14
	v_lshlrev_b32_e32 v13, 10, v13
	v_add_u32_e32 v13, v13, v14
	v_lshlrev_b32_e32 v13, 2, v13
	v_add_u32_e32 v14, 0x10000, v13
	v_add_u32_e32 v15, 0x20000, v13
	v_add_u32_e32 v16, 0x30000, v13
	s_nop 7
	global_store_dwordx4 v13, a[0:3], s[8:9]
	global_store_dwordx4 v13, a[4:7], s[8:9] offset:64
	global_store_dwordx4 v14, a[8:11], s[8:9]
	global_store_dwordx4 v14, a[12:15], s[8:9] offset:64
	global_store_dwordx4 v15, a[16:19], s[8:9]
	global_store_dwordx4 v15, a[20:23], s[8:9] offset:64
	global_store_dwordx4 v16, a[24:27], s[8:9]
	global_store_dwordx4 v16, a[28:31], s[8:9] offset:64
	s_endpgm
	.p2alignl 8, 3212836864
